# baseline (speedup 1.0000x reference)
.LBB1_8:
	s_or_b64 exec, exec, s[2:3]
	v_lshlrev_b32_e32 v23, 3, v0
	v_mov_b32_e32 v22, 0x3c00
	v_and_b32_e32 v23, 0x3f8, v23
	v_cvt_pk_f16_f32 v9, v8, v9
	v_cvt_pk_f16_f32 v8, v6, v7
	v_mul_u32_u24_e32 v6, 0x410, v25
	s_mov_b32 s5, 0x1f800
	v_cndmask_b32_e64 v22, 0, v22, s[0:1]
	v_add3_u32 v6, v6, v23, s5
	v_cvt_pk_f16_f32 v5, v4, v5
	v_cvt_pk_f16_f32 v4, v2, v3
	v_cvt_pk_f16_f32 v3, v16, v17
	v_cvt_pk_f16_f32 v2, v14, v15
	v_mov_b32_e32 v39, 0
	s_movk_i32 s4, 0x140
	v_lshrrev_b32_e32 v84, 5, v85
	ds_write_b64 v6, v[2:3] offset:16640
	v_cvt_pk_f16_f32 v3, v12, v13
	v_cvt_pk_f16_f32 v2, v10, v11
	v_pack_b32_f16 v38, v22, 0
	v_mov_b32_e32 v40, v39
	v_mov_b32_e32 v41, v39
	v_cmp_gt_u32_e32 vcc, s4, v0
	ds_write_b64 v6, v[8:9]
	ds_write_b64 v6, v[4:5] offset:8320
	ds_write_b64 v6, v[2:3] offset:24960
	s_waitcnt lgkmcnt(0)
	s_barrier
	s_and_saveexec_b64 s[2:3], vcc
	s_cbranch_execz .LBB1_10
	s_setprio 3
	s_and_b64 s[6:7], s[6:7], exec
	s_cselect_b32 s6, 5, 0
	v_add_u32_e32 v42, s6, v24
	v_mul_u32_u24_e32 v2, 0x840, v42
	v_or_b32_e32 v2, v2, v85
	v_lshlrev_b32_e32 v48, 4, v2
	v_mov_b32_e32 v49, v39
	v_lshl_add_u64 v[44:45], s[18:19], 0, v[48:49]
	v_add_co_u32_e32 v2, vcc, 0x8000, v44
	v_mul_u32_u24_e32 v6, 0x410, v83
	s_nop 0
	v_addc_co_u32_e32 v3, vcc, 0, v45, vcc
	global_load_dwordx4 v[2:5], v[2:3], off
	s_nop 0
	global_load_dwordx4 v[22:25], v48, s[18:19]
	global_load_dwordx4 v[86:89], v48, s[18:19] offset:1024
	global_load_dwordx4 v[30:33], v48, s[18:19] offset:2048
	v_lshlrev_b32_e32 v7, 4, v84
	v_add3_u32 v102, v6, v7, s5
	ds_read_b128 v[90:93], v102
	ds_read_b128 v[94:97], v102 offset:32
	s_movk_i32 s6, 0x7000
	v_add_co_u32_e32 v98, vcc, s6, v44
	s_movk_i32 s5, 0x2000
	s_nop 0
	v_addc_co_u32_e32 v99, vcc, 0, v45, vcc
	global_load_dwordx4 v[26:29], v[98:99], off offset:3072
	s_waitcnt vmcnt(4)
	v_mfma_f32_32x32x16_f16 v[2:17], v[2:5], v[38:41], 0
	s_waitcnt vmcnt(3) lgkmcnt(1)
	v_mfma_f32_32x32x16_f16 v[2:17], v[22:25], v[90:93], v[2:17]
	global_load_dwordx4 v[22:25], v48, s[18:19] offset:3072
	v_add_co_u32_e32 v48, vcc, s5, v44
	s_movk_i32 s5, 0x1000
	s_nop 0
	v_addc_co_u32_e32 v49, vcc, 0, v45, vcc
	s_waitcnt vmcnt(3) lgkmcnt(0)
	v_mfma_f32_32x32x16_f16 v[2:17], v[86:89], v[94:97], v[2:17]
	ds_read_b128 v[86:89], v102 offset:64
	ds_read_b128 v[90:93], v102 offset:96
	v_add_co_u32_e32 v94, vcc, s5, v44
	s_movk_i32 s5, 0x3000
	s_nop 0
	v_addc_co_u32_e32 v95, vcc, 0, v45, vcc
	v_add_co_u32_e32 v100, vcc, s5, v44
	s_waitcnt vmcnt(2) lgkmcnt(1)
	v_mfma_f32_32x32x16_f16 v[2:17], v[30:33], v[86:89], v[2:17]
	global_load_dwordx4 v[30:33], v[48:49], off offset:-4096
	v_addc_co_u32_e32 v101, vcc, 0, v45, vcc
	s_movk_i32 s5, 0x4000
	s_waitcnt vmcnt(1) lgkmcnt(0)
	v_mfma_f32_32x32x16_f16 v[2:17], v[22:25], v[90:93], v[2:17]
	global_load_dwordx4 v[22:25], v[94:95], off offset:1024
	ds_read_b128 v[86:89], v102 offset:128
	ds_read_b128 v[90:93], v102 offset:160
	s_waitcnt vmcnt(1) lgkmcnt(1)
	v_mfma_f32_32x32x16_f16 v[2:17], v[30:33], v[86:89], v[2:17]
	global_load_dwordx4 v[30:33], v[94:95], off offset:2048
	s_waitcnt vmcnt(1) lgkmcnt(0)
	v_mfma_f32_32x32x16_f16 v[2:17], v[22:25], v[90:93], v[2:17]
	global_load_dwordx4 v[22:25], v[94:95], off offset:3072
	ds_read_b128 v[86:89], v102 offset:192
	ds_read_b128 v[90:93], v102 offset:224
	s_waitcnt vmcnt(1) lgkmcnt(1)
	v_mfma_f32_32x32x16_f16 v[2:17], v[30:33], v[86:89], v[2:17]
	global_load_dwordx4 v[30:33], v[48:49], off
	global_load_dwordx4 v[86:89], v[100:101], off offset:1024
	s_waitcnt vmcnt(2) lgkmcnt(0)
	v_mfma_f32_32x32x16_f16 v[2:17], v[22:25], v[90:93], v[2:17]
	global_load_dwordx4 v[22:25], v[48:49], off offset:1024
	ds_read_b128 v[90:93], v102 offset:256
	ds_read_b128 v[94:97], v102 offset:288
	s_waitcnt vmcnt(2) lgkmcnt(1)
	v_mfma_f32_32x32x16_f16 v[2:17], v[30:33], v[90:93], v[2:17]
	global_load_dwordx4 v[30:33], v[48:49], off offset:2048
	s_waitcnt vmcnt(1) lgkmcnt(0)
	v_mfma_f32_32x32x16_f16 v[2:17], v[22:25], v[94:97], v[2:17]
	global_load_dwordx4 v[22:25], v[48:49], off offset:3072
	ds_read_b128 v[90:93], v102 offset:320
	ds_read_b128 v[94:97], v102 offset:352
	v_add_co_u32_e32 v48, vcc, s5, v44
	s_movk_i32 s5, 0x6000
	s_nop 0
	v_addc_co_u32_e32 v49, vcc, 0, v45, vcc
	s_waitcnt vmcnt(1) lgkmcnt(1)
	v_mfma_f32_32x32x16_f16 v[2:17], v[30:33], v[90:93], v[2:17]
	s_waitcnt vmcnt(0) lgkmcnt(0)
	v_mfma_f32_32x32x16_f16 v[2:17], v[22:25], v[94:97], v[2:17]
	global_load_dwordx4 v[22:25], v[48:49], off offset:-4096
	ds_read_b128 v[30:33], v102 offset:384
	ds_read_b128 v[90:93], v102 offset:416
	global_load_dwordx4 v[94:97], v[48:49], off
	s_waitcnt vmcnt(1) lgkmcnt(1)
	v_mfma_f32_32x32x16_f16 v[2:17], v[22:25], v[30:33], v[2:17]
	global_load_dwordx4 v[22:25], v[100:101], off offset:2048
	global_load_dwordx4 v[30:33], v[100:101], off offset:3072
	s_waitcnt lgkmcnt(0)
	v_mfma_f32_32x32x16_f16 v[2:17], v[86:89], v[90:93], v[2:17]
	ds_read_b128 v[86:89], v102 offset:448
	ds_read_b128 v[90:93], v102 offset:480
	s_waitcnt vmcnt(1) lgkmcnt(1)
	v_mfma_f32_32x32x16_f16 v[2:17], v[22:25], v[86:89], v[2:17]
	global_load_dwordx4 v[22:25], v[48:49], off offset:1024
	s_waitcnt vmcnt(1) lgkmcnt(0)
	v_mfma_f32_32x32x16_f16 v[2:17], v[30:33], v[90:93], v[2:17]
	global_load_dwordx4 v[30:33], v[48:49], off offset:2048
	ds_read_b128 v[86:89], v102 offset:512
	ds_read_b128 v[90:93], v102 offset:544
	s_waitcnt lgkmcnt(1)
	v_mfma_f32_32x32x16_f16 v[2:17], v[94:97], v[86:89], v[2:17]
	global_load_dwordx4 v[86:89], v[48:49], off offset:3072
	v_add_co_u32_e32 v48, vcc, s5, v44
	s_movk_i32 s5, 0x5000
	s_nop 0
	v_addc_co_u32_e32 v49, vcc, 0, v45, vcc
	v_add_co_u32_e32 v44, vcc, s5, v44
	s_waitcnt vmcnt(2) lgkmcnt(0)
	v_mfma_f32_32x32x16_f16 v[2:17], v[22:25], v[90:93], v[2:17]
	ds_read_b128 v[22:25], v102 offset:576
	ds_read_b128 v[90:93], v102 offset:608
	v_addc_co_u32_e32 v45, vcc, 0, v45, vcc
	s_waitcnt vmcnt(1) lgkmcnt(1)
	v_mfma_f32_32x32x16_f16 v[2:17], v[30:33], v[22:25], v[2:17]
	global_load_dwordx4 v[22:25], v[48:49], off offset:-4096
	global_load_dwordx4 v[30:33], v[44:45], off offset:1024
	s_waitcnt vmcnt(2) lgkmcnt(0)
	v_mfma_f32_32x32x16_f16 v[2:17], v[86:89], v[90:93], v[2:17]
	ds_read_b128 v[86:89], v102 offset:640
	ds_read_b128 v[90:93], v102 offset:672
	s_waitcnt vmcnt(1) lgkmcnt(1)
	v_mfma_f32_32x32x16_f16 v[2:17], v[22:25], v[86:89], v[2:17]
	global_load_dwordx4 v[22:25], v[44:45], off offset:2048
	s_waitcnt vmcnt(1) lgkmcnt(0)
	v_mfma_f32_32x32x16_f16 v[2:17], v[30:33], v[90:93], v[2:17]
	global_load_dwordx4 v[30:33], v[44:45], off offset:3072
	ds_read_b128 v[86:89], v102 offset:704
	ds_read_b128 v[90:93], v102 offset:736
	v_or_b32_e32 v44, s28, v83
	v_mov_b32_e32 v45, v39
	s_waitcnt vmcnt(1) lgkmcnt(1)
	v_mfma_f32_32x32x16_f16 v[2:17], v[22:25], v[86:89], v[2:17]
	global_load_dwordx4 v[22:25], v[48:49], off
	global_load_dwordx4 v[86:89], v[98:99], off
	s_waitcnt vmcnt(2) lgkmcnt(0)
	v_mfma_f32_32x32x16_f16 v[2:17], v[30:33], v[90:93], v[2:17]
	global_load_dwordx4 v[30:33], v[48:49], off offset:1024
	ds_read_b128 v[90:93], v102 offset:768
	ds_read_b128 v[94:97], v102 offset:800
	s_waitcnt vmcnt(2) lgkmcnt(1)
	v_mfma_f32_32x32x16_f16 v[2:17], v[22:25], v[90:93], v[2:17]
	global_load_dwordx4 v[22:25], v[48:49], off offset:2048
	s_waitcnt vmcnt(1) lgkmcnt(0)
	v_mfma_f32_32x32x16_f16 v[2:17], v[30:33], v[94:97], v[2:17]
	global_load_dwordx4 v[30:33], v[48:49], off offset:3072
	ds_read_b128 v[90:93], v102 offset:832
	ds_read_b128 v[94:97], v102 offset:864
	v_lshlrev_b32_e32 v48, 3, v84
	v_mov_b32_e32 v49, v39
	s_waitcnt vmcnt(1) lgkmcnt(1)
	v_mfma_f32_32x32x16_f16 v[2:17], v[22:25], v[90:93], v[2:17]
	global_load_dwordx4 v[22:25], v[98:99], off offset:1024
	s_waitcnt vmcnt(1) lgkmcnt(0)
	v_mfma_f32_32x32x16_f16 v[2:17], v[30:33], v[94:97], v[2:17]
	ds_read_b128 v[30:33], v102 offset:896
	ds_read_b128 v[90:93], v102 offset:928
	s_waitcnt lgkmcnt(1)
	v_mfma_f32_32x32x16_f16 v[2:17], v[86:89], v[30:33], v[2:17]
	global_load_dwordx4 v[30:33], v[98:99], off offset:2048
	ds_read_b128 v[86:89], v102 offset:992
	s_waitcnt vmcnt(1) lgkmcnt(1)
	v_mfma_f32_32x32x16_f16 v[2:17], v[22:25], v[90:93], v[2:17]
	ds_read_b128 v[22:25], v102 offset:960
	s_waitcnt vmcnt(0) lgkmcnt(0)
	v_mfma_f32_32x32x16_f16 v[2:17], v[30:33], v[22:25], v[2:17]
	v_mul_lo_u32 v22, v44, s4
	v_ashrrev_i32_e32 v23, 31, v22
	v_lshl_add_u64 v[22:23], v[22:23], 1, s[20:21]
	v_lshlrev_b32_e32 v44, 6, v42
	v_lshl_add_u64 v[22:23], v[22:23], 0, v[44:45]
	v_lshl_add_u64 v[22:23], v[22:23], 0, v[48:49]
	v_mfma_f32_32x32x16_f16 v[2:17], v[26:29], v[86:89], v[2:17]
	s_nop 11
	v_max_f32_e32 v2, v2, v2
	v_max_f32_e32 v3, v3, v3
	v_max_f32_e32 v4, v4, v4
	v_max_f32_e32 v5, v5, v5
	v_max_f32_e32 v6, v6, v6
	v_max_f32_e32 v7, v7, v7
	v_max_f32_e32 v8, v8, v8
	v_max_f32_e32 v9, v9, v9
	v_max_f32_e32 v10, v10, v10
	v_max_f32_e32 v11, v11, v11
	v_max_f32_e32 v12, v12, v12
	v_max_f32_e32 v13, v13, v13
	v_max_f32_e32 v14, v14, v14
	v_max_f32_e32 v15, v15, v15
	v_max_f32_e32 v16, v16, v16
	v_max_f32_e32 v17, v17, v17
	v_max_f32_e32 v2, 0, v2
	v_max_f32_e32 v24, 0, v3
	v_max_f32_e32 v3, 0, v4
	v_max_f32_e32 v4, 0, v5
	v_max_f32_e32 v6, 0, v6
	v_max_f32_e32 v7, 0, v7
	v_max_f32_e32 v5, 0, v8
	v_max_f32_e32 v8, 0, v9
	v_max_f32_e32 v9, 0, v10
	v_max_f32_e32 v10, 0, v11
	v_max_f32_e32 v11, 0, v12
	v_max_f32_e32 v12, 0, v13
	v_max_f32_e32 v13, 0, v14
	v_max_f32_e32 v14, 0, v15
	v_max_f32_e32 v15, 0, v16
	v_max_f32_e32 v16, 0, v17
	v_cvt_pk_f16_f32 v3, v3, v4
	v_cvt_pk_f16_f32 v2, v2, v24
	v_cvt_pk_f16_f32 v5, v5, v8
	v_cvt_pk_f16_f32 v4, v6, v7
	v_cvt_pk_f16_f32 v7, v11, v12
	v_cvt_pk_f16_f32 v6, v9, v10
	v_cvt_pk_f16_f32 v9, v15, v16
	v_cvt_pk_f16_f32 v8, v13, v14
	global_store_dwordx2 v[22:23], v[2:3], off nt
	global_store_dwordx2 v[22:23], v[4:5], off offset:16 nt
	global_store_dwordx2 v[22:23], v[6:7], off offset:32 nt
	global_store_dwordx2 v[22:23], v[8:9], off offset:48 nt
